# PV-first MLA M segment + diff softmax segment trimmed (running DMA pointers advanced in M, compiler nop pads dropped)
# speedup vs baseline: 1.0446x; 1.0446x over previous
; #define PK4(P, BASE, OUT) do { u32x4 w = {cvtpk(P[BASE + 0], P[BASE + 1]), cvtpk(P[BASE + 2], P[BASE + 3]), cvtpk(P[BASE + 4], P[BASE + 5]), cvtpk(P[BASE + 6], P[BASE + 7])}; \
;     OUT = *reinterpret_cast<bf16x8*>(&w); } while (0)
; __device__ __forceinline__ void smax_tile(f32x16& p0, f32x16& p1, float& mhat, float& l_reg, f32x16 (&o)[4], float* al_l, const bool first, int r32, int hi,
;                                           bf16x8& pa0, bf16x8& pa1, bf16x8& pa2, bf16x8& pa3) {
;     ...
; #pragma unroll
;     for (int r = 0; r < 16; ++r) p0[r] = __builtin_amdgcn_exp2f(p0[r]);
; #pragma unroll
;     for (int r = 0; r < 16; ++r) p1[r] = __builtin_amdgcn_exp2f(p1[r]);
;     float ps = p0[0];
; #pragma unroll
;     for (int r = 1; r < 16; ++r) ps += p0[r];
; #pragma unroll
;     for (int r = 0; r < 16; ++r) ps += p1[r];
;     { auto rr = __builtin_amdgcn_permlane32_swap(__float_as_uint(ps), __float_as_uint(ps), false, false); ps = __uint_as_float(rr[0]) + __uint_as_float(rr[1]); }
;     l_reg += ps;
;     ...
;     PK4(p0, 0, pa0); PK4(p0, 8, pa1); PK4(p1, 0, pa2); PK4(p1, 8, pa3);
.LBB0_651:
	v_exp_f32_e32 v96, v96
	v_exp_f32_e32 v97, v97
	v_exp_f32_e32 v98, v98
	v_exp_f32_e32 v99, v99
	v_exp_f32_e32 v100, v100
	v_exp_f32_e32 v101, v101
	v_add_f32_e32 v128, v96, v97
	v_exp_f32_e32 v102, v102
	v_add_f32_e32 v128, v98, v128
	v_exp_f32_e32 v103, v103
	v_add_f32_e32 v128, v99, v128
	v_exp_f32_e32 v104, v104
	v_add_f32_e32 v128, v100, v128
	v_exp_f32_e32 v105, v105
	v_add_f32_e32 v128, v101, v128
	v_exp_f32_e32 v106, v106
	v_add_f32_e32 v128, v102, v128
	v_exp_f32_e32 v107, v107
	v_add_f32_e32 v128, v103, v128
	v_exp_f32_e32 v108, v108
	v_add_f32_e32 v128, v104, v128
	v_exp_f32_e32 v109, v109
	v_add_f32_e32 v128, v105, v128
	v_exp_f32_e32 v110, v110
	v_add_f32_e32 v128, v106, v128
	v_exp_f32_e32 v111, v111
	v_add_f32_e32 v128, v107, v128
	v_exp_f32_e32 v80, v80
	v_add_f32_e32 v128, v108, v128
	v_exp_f32_e32 v81, v81
	v_add_f32_e32 v128, v109, v128
	v_exp_f32_e32 v82, v82
	v_add_f32_e32 v128, v110, v128
	v_exp_f32_e32 v83, v83
	v_add_f32_e32 v128, v111, v128
	v_exp_f32_e32 v84, v84
	v_add_f32_e32 v128, v80, v128
	v_exp_f32_e32 v85, v85
	v_add_f32_e32 v128, v81, v128
	v_exp_f32_e32 v86, v86
	v_add_f32_e32 v128, v82, v128
	v_exp_f32_e32 v87, v87
	v_add_f32_e32 v128, v83, v128
	v_exp_f32_e32 v88, v88
	v_add_f32_e32 v128, v84, v128
	v_exp_f32_e32 v89, v89
	v_add_f32_e32 v128, v85, v128
	v_exp_f32_e32 v90, v90
	v_add_f32_e32 v128, v86, v128
	v_exp_f32_e32 v91, v91
	v_add_f32_e32 v128, v87, v128
	v_exp_f32_e32 v92, v92
	v_add_f32_e32 v128, v88, v128
	v_exp_f32_e32 v93, v93
	v_add_f32_e32 v128, v89, v128
	v_exp_f32_e32 v94, v94
	v_add_f32_e32 v128, v90, v128
	v_exp_f32_e32 v95, v95
	v_add_f32_e32 v128, v91, v128
	v_add_f32_e32 v128, v92, v128
	v_add_f32_e32 v128, v93, v128
	v_add_f32_e32 v128, v94, v128
	v_add_f32_e32 v128, v95, v128
	v_mov_b32_e32 v129, v128
	s_nop 1
	v_permlane32_swap_b32_e32 v128, v129
	v_add_f32_e32 v128, v128, v129
	s_addk_i32 s87, 0xc000
	v_add_f32_e32 v159, v159, v128
	v_cvt_pk_bf16_f32 v162, v96, v97
	v_cvt_pk_bf16_f32 v163, v98, v99
	v_cvt_pk_bf16_f32 v164, v100, v101
	v_cvt_pk_bf16_f32 v165, v102, v103
	v_cvt_pk_bf16_f32 v166, v104, v105
	v_cvt_pk_bf16_f32 v167, v106, v107
	v_cvt_pk_bf16_f32 v168, v108, v109
	v_cvt_pk_bf16_f32 v169, v110, v111
	v_cvt_pk_bf16_f32 v132, v80, v81
	v_cvt_pk_bf16_f32 v133, v82, v83
	v_cvt_pk_bf16_f32 v134, v84, v85
	v_cvt_pk_bf16_f32 v135, v86, v87
	v_cvt_pk_bf16_f32 v128, v88, v89
	v_cvt_pk_bf16_f32 v129, v90, v91
	v_cvt_pk_bf16_f32 v130, v92, v93
	v_cvt_pk_bf16_f32 v131, v94, v95
	s_cmp_lg_u32 s86, 0
	s_waitcnt lgkmcnt(0)
	s_barrier
; #define SBAR() __builtin_amdgcn_sched_barrier(0)
; __device__ __forceinline__ void smax_tile(f32x16& p0, f32x16& p1, float& mhat, float& l_reg, f32x16 (&o)[4], float* al_l, const bool first, int r32, int hi,
;                                           bf16x8& pa0, bf16x8& pa1, bf16x8& pa2, bf16x8& pa3) {
;     float a = vmax3(p0[0], p0[1], p1[0]), b = vmax3(p0[2], p0[3], p1[1]); a = vmax3(a, p1[2], p1[3]);
; #pragma unroll
; template <int DQK, bool HASQK, bool HASPV, int J>
; __device__ __forceinline__ void slot_read(bf16x8 (&kf)[DQK / 16][2], s16x4 (&vf)[4][8], const int (&ka_)[4], int vb_) {
;     constexpr int NQS = HASQK ? 2 * (DQK / 16) : 0, NS = NQS + (HASPV ? 16 : 0);
;     if constexpr (J < NQS) { constexpr int d0 = J >> 1, h = J & 1; dsr128<(d0 >> 2) * 128 + h * 32 * DQK * 2>(kf[d0][h], ka_[d0 & 3]); }
;     else if constexpr (J < NS) { constexpr int q = J - NQS, g = q >> 2, d = q & 3; dstr64<v_rd_off(d, g, 0)>(vf[g][2 * d], vb_); dstr64<v_rd_off(d, g, 1)>(vf[g][2 * d + 1], vb_); }
; }
; template <int DQK, bool HASQK, bool HASPV, int J> ...
;     constexpr int NQS = HASQK ? 2 * (DQK / 16) : 0, NS = NQS + (HASPV ? 16 : 0);
;     if constexpr (J < NS) {
;         constexpr int rd1 = (J + 1 < NS) ? ((J + 1 < NQS) ? 1 : 2) : 0, rd2 = (J + 2 < NS) ? ((J + 2 < NQS) ? 1 : 2) : 0, rd3 = (J + 3 < NS) ? ((J + 3 < NQS) ? 1 : 2) : 0, NW = rd1 + rd2 + rd3;
;     ...
;         if constexpr (J < NQS) { constexpr int d0 = J >> 1, h = J & 1;
;             LWN1(kf[d0][h]); SBAR();
;             if constexpr (h == 0) p0 = __builtin_amdgcn_mfma_f32_32x32x16_bf16(kf[d0][0], qr[d0], (d0 == 0) ? negm : p0, 0, 0, 0);
;             else p1 = __builtin_amdgcn_mfma_f32_32x32x16_bf16(kf[d0][1], qr[d0], (d0 == 0) ? negm : p1, 0, 0, 0);
;         } else { constexpr int q = J - NQS, g = q >> 2, d = q & 3;
;             LWN2(vf[g][2 * d], vf[g][2 * d + 1]); SBAR();
;             o[d] = __builtin_amdgcn_mfma_f32_32x32x16_bf16(pa[g], (bf16x8){vf[g][2 * d][0], vf[g][2 * d][1], vf[g][2 * d][2], vf[g][2 * d][3], vf[g][2 * d + 1][0], vf[g][2 * d + 1][1], vf[g][2 * d + 1][2], vf[g][2 * d + 1][3]}, o[d], 0, 0, 0);
;         }
;     ...
;         SBAR();
;         slot_read<DQK, HASQK, HASPV, J + 4>(kf, vf, ka_, vb_);
;         SBAR();
;         slot_run<DQK, HASQK, HASPV, J + 1>(kf, vf, ka_, vb_, qr, p0, p1, negm, o, pa);
;     }
; }
	s_cselect_b32 s46, s87, 0x8000
	s_lshl_b32 s47, s86, 13
	v_add_u32_e32 v81, s47, v141
	v_add_u32_e32 v82, s47, v143
	ds_read_b128 v[170:173], v81 offset:0
	ds_read_b128 v[174:177], v81 offset:0x1000
	ds_read_b128 v[178:181], v82 offset:0
	ds_read_b128 v[182:185], v82 offset:0x1000
	v_xor_b32_e32 v80, 0x80000000, v158
	v_add_u32_e32 v186, s47, v160
	v_add_u32_e32 v187, s47, v161
	v_add_u32_e32 v188, s46, v157
	v_mov_b32_e32 v81, v80
	v_mov_b32_e32 v82, v80
	v_mov_b32_e32 v83, v80
	v_mov_b32_e32 v84, v80
	v_mov_b32_e32 v85, v80
	v_mov_b32_e32 v86, v80
	v_mov_b32_e32 v87, v80
	v_mov_b32_e32 v88, v80
	v_mov_b32_e32 v89, v80
	v_mov_b32_e32 v90, v80
	v_mov_b32_e32 v91, v80
	v_mov_b32_e32 v92, v80
	v_mov_b32_e32 v93, v80
	v_mov_b32_e32 v94, v80
	v_mov_b32_e32 v95, v80
	s_waitcnt lgkmcnt(3)
	s_nop 1
	v_mfma_f32_32x32x16_bf16 v[96:111], v[170:173], v[112:115], v[80:95]
	ds_read_b128 v[170:173], v186 offset:0
	s_waitcnt lgkmcnt(3)
	s_nop 0
	v_mfma_f32_32x32x16_bf16 v[80:95], v[174:177], v[112:115], v[80:95]
	ds_read_b128 v[174:177], v186 offset:0x1000
	s_waitcnt lgkmcnt(3)
	s_nop 0
	v_mfma_f32_32x32x16_bf16 v[96:111], v[178:181], v[116:119], v[96:111]
	ds_read_b128 v[178:181], v187 offset:0
	s_waitcnt lgkmcnt(3)
	s_nop 0
	v_mfma_f32_32x32x16_bf16 v[80:95], v[182:185], v[116:119], v[80:95]
	ds_read_b128 v[182:185], v187 offset:0x1000
	s_waitcnt lgkmcnt(3)
	s_nop 0
	v_mfma_f32_32x32x16_bf16 v[96:111], v[170:173], v[120:123], v[96:111]
	ds_read_b64_tr_b16 v[170:171], v188 offset:0
	ds_read_b64_tr_b16 v[172:173], v188 offset:0x800
	s_waitcnt lgkmcnt(4)
	s_nop 0
	v_mfma_f32_32x32x16_bf16 v[80:95], v[174:177], v[120:123], v[80:95]
	ds_read_b64_tr_b16 v[174:175], v188 offset:0x200
	ds_read_b64_tr_b16 v[176:177], v188 offset:0xa00
	s_waitcnt lgkmcnt(5)
	s_nop 0
	v_mfma_f32_32x32x16_bf16 v[96:111], v[178:181], v[124:127], v[96:111]
	ds_read_b64_tr_b16 v[178:179], v188 offset:0x400
	ds_read_b64_tr_b16 v[180:181], v188 offset:0xc00
	s_waitcnt lgkmcnt(6)
	s_nop 0
	v_mfma_f32_32x32x16_bf16 v[80:95], v[182:185], v[124:127], v[80:95]
	ds_read_b64_tr_b16 v[182:183], v188 offset:0x600
	ds_read_b64_tr_b16 v[184:185], v188 offset:0xe00
	s_waitcnt lgkmcnt(6)
	s_nop 0
	v_mfma_f32_32x32x16_bf16 v[64:79], v[162:165], v[170:173], v[64:79]
	ds_read_b64_tr_b16 v[170:171], v188 offset:0x1000
	ds_read_b64_tr_b16 v[172:173], v188 offset:0x1800
	s_waitcnt lgkmcnt(6)
	s_nop 0
	v_mfma_f32_32x32x16_bf16 v[48:63], v[162:165], v[174:177], v[48:63]
	ds_read_b64_tr_b16 v[174:175], v188 offset:0x1200
	ds_read_b64_tr_b16 v[176:177], v188 offset:0x1a00
	s_waitcnt lgkmcnt(6)
	s_nop 0
	v_mfma_f32_32x32x16_bf16 v[32:47], v[162:165], v[178:181], v[32:47]
	ds_read_b64_tr_b16 v[178:179], v188 offset:0x1400
	ds_read_b64_tr_b16 v[180:181], v188 offset:0x1c00
	s_waitcnt lgkmcnt(6)
	s_nop 0
	v_mfma_f32_32x32x16_bf16 v[16:31], v[162:165], v[182:185], v[16:31]
	ds_read_b64_tr_b16 v[162:163], v188 offset:0x1600
	ds_read_b64_tr_b16 v[164:165], v188 offset:0x1e00
	s_waitcnt lgkmcnt(6)
	s_nop 0
	v_mfma_f32_32x32x16_bf16 v[64:79], v[166:169], v[170:173], v[64:79]
	ds_read_b64_tr_b16 v[170:171], v188 offset:0x2000
	ds_read_b64_tr_b16 v[172:173], v188 offset:0x2800
	s_waitcnt lgkmcnt(6)
	s_nop 0
	v_mfma_f32_32x32x16_bf16 v[48:63], v[166:169], v[174:177], v[48:63]
	ds_read_b64_tr_b16 v[174:175], v188 offset:0x2200
	ds_read_b64_tr_b16 v[176:177], v188 offset:0x2a00
	s_waitcnt lgkmcnt(6)
	s_nop 0
	v_mfma_f32_32x32x16_bf16 v[32:47], v[166:169], v[178:181], v[32:47]
	ds_read_b64_tr_b16 v[178:179], v188 offset:0x2400
	ds_read_b64_tr_b16 v[180:181], v188 offset:0x2c00
	s_waitcnt lgkmcnt(6)
	s_nop 0
	v_mfma_f32_32x32x16_bf16 v[16:31], v[166:169], v[162:165], v[16:31]
	ds_read_b64_tr_b16 v[162:163], v188 offset:0x2600
	ds_read_b64_tr_b16 v[164:165], v188 offset:0x2e00
	s_waitcnt lgkmcnt(6)
	s_nop 0
	v_mfma_f32_32x32x16_bf16 v[64:79], v[132:135], v[170:173], v[64:79]
	ds_read_b64_tr_b16 v[166:167], v188 offset:0x3000
	ds_read_b64_tr_b16 v[168:169], v188 offset:0x3800
	s_waitcnt lgkmcnt(6)
	s_nop 0
	v_mfma_f32_32x32x16_bf16 v[48:63], v[132:135], v[174:177], v[48:63]
	ds_read_b64_tr_b16 v[170:171], v188 offset:0x3200
	ds_read_b64_tr_b16 v[172:173], v188 offset:0x3a00
	s_waitcnt lgkmcnt(6)
	s_nop 0
	v_mfma_f32_32x32x16_bf16 v[32:47], v[132:135], v[178:181], v[32:47]
	ds_read_b64_tr_b16 v[174:175], v188 offset:0x3400
	ds_read_b64_tr_b16 v[176:177], v188 offset:0x3c00
	s_waitcnt lgkmcnt(6)
	s_nop 0
	v_mfma_f32_32x32x16_bf16 v[16:31], v[132:135], v[162:165], v[16:31]
	ds_read_b64_tr_b16 v[132:133], v188 offset:0x3600
	ds_read_b64_tr_b16 v[134:135], v188 offset:0x3e00
	s_waitcnt lgkmcnt(6)
	s_nop 0
	v_mfma_f32_32x32x16_bf16 v[64:79], v[128:131], v[166:169], v[64:79]
	s_waitcnt lgkmcnt(4)
	s_nop 0
	v_mfma_f32_32x32x16_bf16 v[48:63], v[128:131], v[170:173], v[48:63]
	s_waitcnt lgkmcnt(2)
	s_nop 0
	v_mfma_f32_32x32x16_bf16 v[32:47], v[128:131], v[174:177], v[32:47]
	s_waitcnt lgkmcnt(0)
	s_nop 0
	v_mfma_f32_32x32x16_bf16 v[16:31], v[128:131], v[132:135], v[16:31]
	v_lshl_add_u64 v[144:145], v[144:145], 0, s[28:29]
	v_lshl_add_u64 v[146:147], v[146:147], 0, s[28:29]
	v_lshl_add_u64 v[148:149], v[148:149], 0, s[28:29]
	s_waitcnt vmcnt(0)
	s_add_u32 s44, s44, 0x10000
	s_waitcnt lgkmcnt(0)
	s_barrier
	s_addc_u32 s45, s45, 0
	s_cmp_eq_u32 s44, 0x7f0000
	s_cbranch_scc1 .LBB0_662
.LBB0_652:
	s_cmp_eq_u32 s44, 0x7e0000
	s_cbranch_scc1 .LBB0_654
	s_lshl_b32 s46, s86, 13
	s_addk_i32 s46, 0xe000
	s_cmp_lg_u32 s86, 0
	s_cselect_b32 s46, s46, 0x4000
	s_add_i32 m0, s69, s46
	s_nop 0
	global_load_lds_dwordx4 v[144:145], off
.LBB0_654:
	s_add_i32 s46, s86, 1
	s_cmp_lg_u32 s86, 2
	s_cselect_b32 s86, s46, 0
	s_lshl_b32 s87, s86, 14
	s_add_i32 s46, s68, s87
	s_add_i32 m0, s46, 0x6000
	s_nop 0
	global_load_lds_dwordx4 v[146:147], off
	s_add_i32 m0, s46, 0x6400
	s_nop 0
	global_load_lds_dwordx4 v[148:149], off
	v_max3_f32 v128, v96, v97, v80
	v_max3_f32 v129, v98, v99, v81
	s_cmp_lg_u32 s44, 0
	v_max3_f32 v128, v128, v82, v83
	v_max3_f32 v129, v129, v102, v103
	s_cselect_b64 s[46:47], -1, 0
	v_max3_f32 v128, v128, v100, v101
	v_max3_f32 v129, v129, v86, v87
	s_cmp_eq_u32 s44, 0
	v_max3_f32 v128, v128, v84, v85
	v_max3_f32 v129, v129, v106, v107
	v_max3_f32 v128, v128, v104, v105
	v_max3_f32 v129, v129, v90, v91
	v_max3_f32 v128, v128, v88, v89
	v_max3_f32 v129, v129, v110, v111
	v_max3_f32 v128, v128, v108, v109
	v_max3_f32 v129, v129, v94, v95
	v_max3_f32 v128, v128, v92, v93
	v_max_f32 v128, v128, v129
	v_mov_b32_e32 v129, v128
	s_nop 1
	v_permlane32_swap_b32_e32 v128, v129
	v_max_f32 v128, v128, v129
	s_cbranch_scc1 .LBB0_661
	v_cmp_lt_f32_e32 vcc, s79, v128
	s_mov_b64 s[52:53], 0
	s_cbranch_vccnz .LBB0_660
	s_and_b64 vcc, exec, s[52:53]
	s_cbranch_vccz .LBB0_651
